# speedup vs baseline: 1.0501x; 1.0104x over previous
_Z11prep_kernelPKfS0_S0_S0_S0_S0_S0_S0_S0_PKiPDv8_DF16bS4_PfS5_S5_PiPt:
	s_load_dwordx4 s[16:19], s[0:1], 0x0
	s_load_dwordx4 s[20:23], s[0:1], 0x10
	s_load_dwordx4 s[24:27], s[0:1], 0x20
	s_load_dwordx4 s[28:31], s[0:1], 0x30
	s_load_dwordx4 s[32:35], s[0:1], 0x40
	s_load_dwordx2 s[36:37], s[0:1], 0x80
	v_and_b32_e32 v126, 63, v0
	v_lshrrev_b32_e32 v128, 6, v0
	v_and_b32_e32 v1, 15, v0
	v_bfe_u32 v24, v0, 4, 2
	v_lshl_or_b32 v107, v128, 4, v1
	v_lshlrev_b32_e32 v106, 2, v107
	v_lshlrev_b32_e32 v127, 2, v0
	v_lshlrev_b32_e32 v25, 1, v107
	v_and_b32_e32 v26, 48, v0
	v_mul_u32_u24_e32 v27, 0x440, v24
	v_lshlrev_b32_e32 v120, 4, v0
	v_lshrrev_b32_e32 v58, 5, v0
	v_mul_u32_u24_e32 v58, 0x110, v58
	v_and_b32_e32 v125, 31, v0
	v_lshl_add_u32 v58, v125, 3, v58
	v_add_u32_e32 v124, 0x1b400, v58
	v_mul_u32_u24_e32 v52, 0x110, v1
	v_add_u32_e32 v52, v52, v26
	v_add_u32_e32 v53, 0x1b400, v52
	v_add_u32_e32 v54, 0x1c500, v52
	v_add_u32_e32 v55, v27, v25
	v_add_u32_e32 v55, 0x1c500, v55
	v_mul_u32_u24_e32 v56, 0x110, v107
	v_add_u32_e32 v56, v56, v26
	v_add_u32_e32 v57, 0x8800, v56
	s_lshl_b32 s12, s2, 4
	s_add_i32 s3, s12, 0xfffff800
	s_cmpk_gt_i32 s2, 0x7f
	s_cselect_b64 s[6:7], -1, 0
	s_mov_b32 s48, 0
	s_mov_b32 s49, -1
	v_lshl_or_b32 v123, s2, 3, v128
	v_lshlrev_b32_e32 v123, 12, v123
	v_lshl_add_u32 v123, v126, 4, v123
	s_waitcnt lgkmcnt(0)
	s_cmpk_lt_i32 s2, 0x80
	s_cselect_b32 s38, s16, s18
	s_cselect_b32 s39, s17, s19
	s_cselect_b32 s40, s20, s24
	s_cselect_b32 s41, s21, s25
	s_cselect_b32 s13, s12, s3
	s_cselect_b32 s44, 0x3db504f3, 1.0
	s_lshl_b32 s13, s13, 9
	s_add_u32 s38, s38, s13
	s_addc_u32 s39, s39, 0
	global_load_dwordx4 v[2:5], v120, s[38:39] nt
	s_and_b32 s13, s2, 7
	s_lshl_b32 s14, s13, 13
	v_add_u32_e32 v125, s14, v120
	global_load_dwordx4 v[80:83], v125, s[40:41]
	s_add_i32 s13, s2, 1
	s_and_b32 s13, s13, 7
	s_lshl_b32 s14, s13, 13
	v_add_u32_e32 v125, s14, v120
	global_load_dwordx4 v[84:87], v125, s[40:41]
	s_add_i32 s13, s2, 2
	s_and_b32 s13, s13, 7
	s_lshl_b32 s14, s13, 13
	v_add_u32_e32 v125, s14, v120
	global_load_dwordx4 v[88:91], v125, s[40:41]
	s_add_i32 s13, s2, 3
	s_and_b32 s13, s13, 7
	s_lshl_b32 s14, s13, 13
	v_add_u32_e32 v125, s14, v120
	global_load_dwordx4 v[92:95], v125, s[40:41]
	s_add_i32 s13, s2, 4
	s_and_b32 s13, s13, 7
	s_lshl_b32 s14, s13, 13
	v_add_u32_e32 v125, s14, v120
	global_load_dwordx4 v[96:99], v125, s[40:41]
	s_add_i32 s13, s2, 5
	s_and_b32 s13, s13, 7
	s_lshl_b32 s14, s13, 13
	v_add_u32_e32 v125, s14, v120
	global_load_dwordx4 v[100:103], v125, s[40:41]
	s_add_i32 s13, s2, 6
	s_and_b32 s13, s13, 7
	s_lshl_b32 s14, s13, 13
	v_add_u32_e32 v125, s14, v120
	global_load_dwordx4 v[108:111], v125, s[40:41]
	s_add_i32 s13, s2, 7
	s_and_b32 s13, s13, 7
	s_lshl_b32 s14, s13, 13
	v_add_u32_e32 v125, s14, v120
	global_load_dwordx4 v[112:115], v125, s[40:41]
	global_load_dword v129, v106, s[32:33]
	global_load_dword v130, v106, s[30:31]
	s_and_b64 vcc, exec, s[6:7]
	s_cbranch_vccz .Lp_q
	v_cmp_gt_u32_e32 vcc, 32, v126
	v_mov_b32_e32 v198, 0x3db504f3
	v_mov_b32_e32 v125, s22
	v_mov_b32_e32 v104, s26
	v_cndmask_b32_e32 v198, 1.0, v198, vcc
	v_cndmask_b32_e32 v104, v104, v125, vcc
	v_mov_b32_e32 v125, s23
	v_mov_b32_e32 v105, s27
	v_cndmask_b32_e32 v105, v105, v125, vcc
	v_and_b32_e32 v196, 31, v126
	v_lshlrev_b32_e32 v196, 4, v196
	v_mov_b32_e32 v197, 0
	v_lshl_add_u64 v[104:105], v[104:105], 0, v[196:197]
	global_load_dwordx4 v[116:119], v[104:105], off
	v_lshlrev_b32_e32 v121, 14, v128
	v_lshl_add_u32 v121, v126, 4, v121
	s_and_b32 s13, s2, 15
	s_lshl_b32 s14, s13, 10
	s_add_u32 s46, s28, s14
	s_addc_u32 s47, s29, 0
	global_load_dwordx4 v[132:135], v121, s[46:47]
	s_add_i32 s13, s2, 1
	s_and_b32 s13, s13, 15
	s_lshl_b32 s14, s13, 10
	s_add_u32 s46, s28, s14
	s_addc_u32 s47, s29, 0
	global_load_dwordx4 v[136:139], v121, s[46:47]
	s_add_i32 s13, s2, 2
	s_and_b32 s13, s13, 15
	s_lshl_b32 s14, s13, 10
	s_add_u32 s46, s28, s14
	s_addc_u32 s47, s29, 0
	global_load_dwordx4 v[140:143], v121, s[46:47]
	s_add_i32 s13, s2, 3
	s_and_b32 s13, s13, 15
	s_lshl_b32 s14, s13, 10
	s_add_u32 s46, s28, s14
	s_addc_u32 s47, s29, 0
	global_load_dwordx4 v[144:147], v121, s[46:47]
	s_add_i32 s13, s2, 4
	s_and_b32 s13, s13, 15
	s_lshl_b32 s14, s13, 10
	s_add_u32 s46, s28, s14
	s_addc_u32 s47, s29, 0
	global_load_dwordx4 v[148:151], v121, s[46:47]
	s_add_i32 s13, s2, 5
	s_and_b32 s13, s13, 15
	s_lshl_b32 s14, s13, 10
	s_add_u32 s46, s28, s14
	s_addc_u32 s47, s29, 0
	global_load_dwordx4 v[152:155], v121, s[46:47]
	s_add_i32 s13, s2, 6
	s_and_b32 s13, s13, 15
	s_lshl_b32 s14, s13, 10
	s_add_u32 s46, s28, s14
	s_addc_u32 s47, s29, 0
	global_load_dwordx4 v[156:159], v121, s[46:47]
	s_add_i32 s13, s2, 7
	s_and_b32 s13, s13, 15
	s_lshl_b32 s14, s13, 10
	s_add_u32 s46, s28, s14
	s_addc_u32 s47, s29, 0
	global_load_dwordx4 v[160:163], v121, s[46:47]
	s_add_i32 s13, s2, 8
	s_and_b32 s13, s13, 15
	s_lshl_b32 s14, s13, 10
	s_add_u32 s46, s28, s14
	s_addc_u32 s47, s29, 0
	global_load_dwordx4 v[164:167], v121, s[46:47]
	s_add_i32 s13, s2, 9
	s_and_b32 s13, s13, 15
	s_lshl_b32 s14, s13, 10
	s_add_u32 s46, s28, s14
	s_addc_u32 s47, s29, 0
	global_load_dwordx4 v[168:171], v121, s[46:47]
	s_add_i32 s13, s2, 10
	s_and_b32 s13, s13, 15
	s_lshl_b32 s14, s13, 10
	s_add_u32 s46, s28, s14
	s_addc_u32 s47, s29, 0
	global_load_dwordx4 v[172:175], v121, s[46:47]
	s_add_i32 s13, s2, 11
	s_and_b32 s13, s13, 15
	s_lshl_b32 s14, s13, 10
	s_add_u32 s46, s28, s14
	s_addc_u32 s47, s29, 0
	global_load_dwordx4 v[176:179], v121, s[46:47]
	s_add_i32 s13, s2, 12
	s_and_b32 s13, s13, 15
	s_lshl_b32 s14, s13, 10
	s_add_u32 s46, s28, s14
	s_addc_u32 s47, s29, 0
	global_load_dwordx4 v[180:183], v121, s[46:47]
	s_add_i32 s13, s2, 13
	s_and_b32 s13, s13, 15
	s_lshl_b32 s14, s13, 10
	s_add_u32 s46, s28, s14
	s_addc_u32 s47, s29, 0
	global_load_dwordx4 v[184:187], v121, s[46:47]
	s_add_i32 s13, s2, 14
	s_and_b32 s13, s13, 15
	s_lshl_b32 s14, s13, 10
	s_add_u32 s46, s28, s14
	s_addc_u32 s47, s29, 0
	global_load_dwordx4 v[188:191], v121, s[46:47]
	s_add_i32 s13, s2, 15
	s_and_b32 s13, s13, 15
	s_lshl_b32 s14, s13, 10
	s_add_u32 s46, s28, s14
	s_addc_u32 s47, s29, 0
	global_load_dwordx4 v[192:195], v121, s[46:47]
	v_mul_u32_u24_e32 v59, 0x1040, v128
	v_lshl_add_u32 v59, v126, 2, v59
	v_add_u32_e32 v59, 0x11000, v59
	v_mul_u32_u24_e32 v76, 0x1100, v128
	v_lshl_add_u32 v76, v126, 3, v76
	v_add_u32_e32 v76, 0x8700, v76
	v_lshrrev_b32_e32 v77, 2, v126
	v_mul_u32_u24_e32 v77, 0x104, v77
	v_mul_u32_u24_e32 v125, 0x1040, v128
	v_add_u32_e32 v77, v77, v125
	v_and_b32_e32 v125, 3, v126
	v_lshl_add_u32 v77, v125, 6, v77
	v_add_u32_e32 v77, 0x11000, v77
	s_waitcnt vmcnt(27)
	v_cvt_pk_bf16_f32 v12, v2, v3
	v_cvt_pk_bf16_f32 v13, v4, v5
	ds_write_b64 v124, v[12:13]
	s_waitcnt vmcnt(26)
	v_cvt_pk_bf16_f32 v6, v80, v81
	v_cvt_pk_bf16_f32 v7, v82, v83
	s_and_b32 s13, s2, 7
	s_mul_i32 s14, s13, 0x1100
	v_add_u32_e32 v125, s14, v58
	ds_write_b64 v125, v[6:7]
	s_waitcnt vmcnt(25)
	v_cvt_pk_bf16_f32 v8, v84, v85
	v_cvt_pk_bf16_f32 v9, v86, v87
	s_add_i32 s13, s2, 1
	s_and_b32 s13, s13, 7
	s_mul_i32 s14, s13, 0x1100
	v_add_u32_e32 v10, s14, v58
	ds_write_b64 v10, v[8:9]
	s_waitcnt vmcnt(24)
	v_cvt_pk_bf16_f32 v6, v88, v89
	v_cvt_pk_bf16_f32 v7, v90, v91
	s_add_i32 s13, s2, 2
	s_and_b32 s13, s13, 7
	s_mul_i32 s14, s13, 0x1100
	v_add_u32_e32 v125, s14, v58
	ds_write_b64 v125, v[6:7]
	s_waitcnt vmcnt(23)
	v_cvt_pk_bf16_f32 v8, v92, v93
	v_cvt_pk_bf16_f32 v9, v94, v95
	s_add_i32 s13, s2, 3
	s_and_b32 s13, s13, 7
	s_mul_i32 s14, s13, 0x1100
	v_add_u32_e32 v10, s14, v58
	ds_write_b64 v10, v[8:9]
	s_waitcnt vmcnt(22)
	v_cvt_pk_bf16_f32 v6, v96, v97
	v_cvt_pk_bf16_f32 v7, v98, v99
	s_add_i32 s13, s2, 4
	s_and_b32 s13, s13, 7
	s_mul_i32 s14, s13, 0x1100
	v_add_u32_e32 v125, s14, v58
	ds_write_b64 v125, v[6:7]
	s_waitcnt vmcnt(21)
	v_cvt_pk_bf16_f32 v8, v100, v101
	v_cvt_pk_bf16_f32 v9, v102, v103
	s_add_i32 s13, s2, 5
	s_and_b32 s13, s13, 7
	s_mul_i32 s14, s13, 0x1100
	v_add_u32_e32 v10, s14, v58
	ds_write_b64 v10, v[8:9]
	s_waitcnt vmcnt(20)
	v_cvt_pk_bf16_f32 v6, v108, v109
	v_cvt_pk_bf16_f32 v7, v110, v111
	s_add_i32 s13, s2, 6
	s_and_b32 s13, s13, 7
	s_mul_i32 s14, s13, 0x1100
	v_add_u32_e32 v125, s14, v58
	ds_write_b64 v125, v[6:7]
	s_waitcnt vmcnt(19)
	v_cvt_pk_bf16_f32 v8, v112, v113
	v_cvt_pk_bf16_f32 v9, v114, v115
	s_add_i32 s13, s2, 7
	s_and_b32 s13, s13, 7
	s_mul_i32 s14, s13, 0x1100
	v_add_u32_e32 v10, s14, v58
	ds_write_b64 v10, v[8:9]
	s_waitcnt vmcnt(16)
	v_pk_mul_f32 v[116:117], v[198:199], v[116:117] op_sel_hi:[0,1]
	v_pk_mul_f32 v[118:119], v[198:199], v[118:119] op_sel_hi:[0,1]
	s_waitcnt vmcnt(15)
	v_mul_f32_e32 v6, v117, v133
	v_mul_f32_e32 v7, v119, v135
	v_fmac_f32_e32 v6, v116, v132
	v_fmac_f32_e32 v7, v118, v134
	s_and_b32 s13, s2, 15
	s_mul_i32 s14, s13, 0x104
	s_mul_i32 s15, s13, 0x110
	v_add_f32_e32 v6, v6, v7
	v_add_u32_e32 v125, s14, v59
	ds_write_b32 v125, v6
	v_cvt_pk_bf16_f32 v8, v132, v133
	v_cvt_pk_bf16_f32 v9, v134, v135
	v_add_u32_e32 v10, s15, v76
	s_mov_b64 exec, s[48:49]
	ds_write_b64 v10, v[8:9]
	s_mov_b64 exec, -1
	s_waitcnt vmcnt(14)
	v_mul_f32_e32 v11, v117, v137
	v_mul_f32_e32 v15, v119, v139
	v_fmac_f32_e32 v11, v116, v136
	v_fmac_f32_e32 v15, v118, v138
	s_add_i32 s13, s2, 1
	s_and_b32 s13, s13, 15
	s_mul_i32 s14, s13, 0x104
	s_mul_i32 s15, s13, 0x110
	v_add_f32_e32 v11, v11, v15
	v_add_u32_e32 v16, s14, v59
	ds_write_b32 v16, v11
	v_cvt_pk_bf16_f32 v12, v136, v137
	v_cvt_pk_bf16_f32 v13, v138, v139
	v_add_u32_e32 v14, s15, v76
	s_mov_b64 exec, s[48:49]
	ds_write_b64 v14, v[12:13]
	s_mov_b64 exec, -1
	s_waitcnt vmcnt(13)
	v_mul_f32_e32 v6, v117, v141
	v_mul_f32_e32 v7, v119, v143
	v_fmac_f32_e32 v6, v116, v140
	v_fmac_f32_e32 v7, v118, v142
	s_add_i32 s13, s2, 2
	s_and_b32 s13, s13, 15
	s_mul_i32 s14, s13, 0x104
	s_mul_i32 s15, s13, 0x110
	v_add_f32_e32 v6, v6, v7
	v_add_u32_e32 v125, s14, v59
	ds_write_b32 v125, v6
	v_cvt_pk_bf16_f32 v8, v140, v141
	v_cvt_pk_bf16_f32 v9, v142, v143
	v_add_u32_e32 v10, s15, v76
	s_mov_b64 exec, s[48:49]
	ds_write_b64 v10, v[8:9]
	s_mov_b64 exec, -1
	s_waitcnt vmcnt(12)
	v_mul_f32_e32 v11, v117, v145
	v_mul_f32_e32 v15, v119, v147
	v_fmac_f32_e32 v11, v116, v144
	v_fmac_f32_e32 v15, v118, v146
	s_add_i32 s13, s2, 3
	s_and_b32 s13, s13, 15
	s_mul_i32 s14, s13, 0x104
	s_mul_i32 s15, s13, 0x110
	v_add_f32_e32 v11, v11, v15
	v_add_u32_e32 v16, s14, v59
	ds_write_b32 v16, v11
	v_cvt_pk_bf16_f32 v12, v144, v145
	v_cvt_pk_bf16_f32 v13, v146, v147
	v_add_u32_e32 v14, s15, v76
	s_mov_b64 exec, s[48:49]
	ds_write_b64 v14, v[12:13]
	s_mov_b64 exec, -1
	s_waitcnt vmcnt(11)
	v_mul_f32_e32 v6, v117, v149
	v_mul_f32_e32 v7, v119, v151
	v_fmac_f32_e32 v6, v116, v148
	v_fmac_f32_e32 v7, v118, v150
	s_add_i32 s13, s2, 4
	s_and_b32 s13, s13, 15
	s_mul_i32 s14, s13, 0x104
	s_mul_i32 s15, s13, 0x110
	v_add_f32_e32 v6, v6, v7
	v_add_u32_e32 v125, s14, v59
	ds_write_b32 v125, v6
	v_cvt_pk_bf16_f32 v8, v148, v149
	v_cvt_pk_bf16_f32 v9, v150, v151
	v_add_u32_e32 v10, s15, v76
	s_mov_b64 exec, s[48:49]
	ds_write_b64 v10, v[8:9]
	s_mov_b64 exec, -1
	s_waitcnt vmcnt(10)
	v_mul_f32_e32 v11, v117, v153
	v_mul_f32_e32 v15, v119, v155
	v_fmac_f32_e32 v11, v116, v152
	v_fmac_f32_e32 v15, v118, v154
	s_add_i32 s13, s2, 5
	s_and_b32 s13, s13, 15
	s_mul_i32 s14, s13, 0x104
	s_mul_i32 s15, s13, 0x110
	v_add_f32_e32 v11, v11, v15
	v_add_u32_e32 v16, s14, v59
	ds_write_b32 v16, v11
	v_cvt_pk_bf16_f32 v12, v152, v153
	v_cvt_pk_bf16_f32 v13, v154, v155
	v_add_u32_e32 v14, s15, v76
	s_mov_b64 exec, s[48:49]
	ds_write_b64 v14, v[12:13]
	s_mov_b64 exec, -1
	s_waitcnt vmcnt(9)
	v_mul_f32_e32 v6, v117, v157
	v_mul_f32_e32 v7, v119, v159
	v_fmac_f32_e32 v6, v116, v156
	v_fmac_f32_e32 v7, v118, v158
	s_add_i32 s13, s2, 6
	s_and_b32 s13, s13, 15
	s_mul_i32 s14, s13, 0x104
	s_mul_i32 s15, s13, 0x110
	v_add_f32_e32 v6, v6, v7
	v_add_u32_e32 v125, s14, v59
	ds_write_b32 v125, v6
	v_cvt_pk_bf16_f32 v8, v156, v157
	v_cvt_pk_bf16_f32 v9, v158, v159
	v_add_u32_e32 v10, s15, v76
	s_mov_b64 exec, s[48:49]
	ds_write_b64 v10, v[8:9]
	s_mov_b64 exec, -1
	s_waitcnt vmcnt(8)
	v_mul_f32_e32 v11, v117, v161
	v_mul_f32_e32 v15, v119, v163
	v_fmac_f32_e32 v11, v116, v160
	v_fmac_f32_e32 v15, v118, v162
	s_add_i32 s13, s2, 7
	s_and_b32 s13, s13, 15
	s_mul_i32 s14, s13, 0x104
	s_mul_i32 s15, s13, 0x110
	v_add_f32_e32 v11, v11, v15
	v_add_u32_e32 v16, s14, v59
	ds_write_b32 v16, v11
	v_cvt_pk_bf16_f32 v12, v160, v161
	v_cvt_pk_bf16_f32 v13, v162, v163
	v_add_u32_e32 v14, s15, v76
	s_mov_b64 exec, s[48:49]
	ds_write_b64 v14, v[12:13]
	s_mov_b64 exec, -1
	s_waitcnt vmcnt(7)
	v_mul_f32_e32 v6, v117, v165
	v_mul_f32_e32 v7, v119, v167
	v_fmac_f32_e32 v6, v116, v164
	v_fmac_f32_e32 v7, v118, v166
	s_add_i32 s13, s2, 8
	s_and_b32 s13, s13, 15
	s_mul_i32 s14, s13, 0x104
	s_mul_i32 s15, s13, 0x110
	v_add_f32_e32 v6, v6, v7
	v_add_u32_e32 v125, s14, v59
	ds_write_b32 v125, v6
	v_cvt_pk_bf16_f32 v8, v164, v165
	v_cvt_pk_bf16_f32 v9, v166, v167
	v_add_u32_e32 v10, s15, v76
	s_mov_b64 exec, s[48:49]
	ds_write_b64 v10, v[8:9]
	s_mov_b64 exec, -1
	s_waitcnt vmcnt(6)
	v_mul_f32_e32 v11, v117, v169
	v_mul_f32_e32 v15, v119, v171
	v_fmac_f32_e32 v11, v116, v168
	v_fmac_f32_e32 v15, v118, v170
	s_add_i32 s13, s2, 9
	s_and_b32 s13, s13, 15
	s_mul_i32 s14, s13, 0x104
	s_mul_i32 s15, s13, 0x110
	v_add_f32_e32 v11, v11, v15
	v_add_u32_e32 v16, s14, v59
	ds_write_b32 v16, v11
	v_cvt_pk_bf16_f32 v12, v168, v169
	v_cvt_pk_bf16_f32 v13, v170, v171
	v_add_u32_e32 v14, s15, v76
	s_mov_b64 exec, s[48:49]
	ds_write_b64 v14, v[12:13]
	s_mov_b64 exec, -1
	s_waitcnt vmcnt(5)
	v_mul_f32_e32 v6, v117, v173
	v_mul_f32_e32 v7, v119, v175
	v_fmac_f32_e32 v6, v116, v172
	v_fmac_f32_e32 v7, v118, v174
	s_add_i32 s13, s2, 10
	s_and_b32 s13, s13, 15
	s_mul_i32 s14, s13, 0x104
	s_mul_i32 s15, s13, 0x110
	v_add_f32_e32 v6, v6, v7
	v_add_u32_e32 v125, s14, v59
	ds_write_b32 v125, v6
	v_cvt_pk_bf16_f32 v8, v172, v173
	v_cvt_pk_bf16_f32 v9, v174, v175
	v_add_u32_e32 v10, s15, v76
	s_mov_b64 exec, s[48:49]
	ds_write_b64 v10, v[8:9]
	s_mov_b64 exec, -1
	s_waitcnt vmcnt(4)
	v_mul_f32_e32 v11, v117, v177
	v_mul_f32_e32 v15, v119, v179
	v_fmac_f32_e32 v11, v116, v176
	v_fmac_f32_e32 v15, v118, v178
	s_add_i32 s13, s2, 11
	s_and_b32 s13, s13, 15
	s_mul_i32 s14, s13, 0x104
	s_mul_i32 s15, s13, 0x110
	v_add_f32_e32 v11, v11, v15
	v_add_u32_e32 v16, s14, v59
	ds_write_b32 v16, v11
	v_cvt_pk_bf16_f32 v12, v176, v177
	v_cvt_pk_bf16_f32 v13, v178, v179
	v_add_u32_e32 v14, s15, v76
	s_mov_b64 exec, s[48:49]
	ds_write_b64 v14, v[12:13]
	s_mov_b64 exec, -1
	s_waitcnt vmcnt(3)
	v_mul_f32_e32 v6, v117, v181
	v_mul_f32_e32 v7, v119, v183
	v_fmac_f32_e32 v6, v116, v180
	v_fmac_f32_e32 v7, v118, v182
	s_add_i32 s13, s2, 12
	s_and_b32 s13, s13, 15
	s_mul_i32 s14, s13, 0x104
	s_mul_i32 s15, s13, 0x110
	v_add_f32_e32 v6, v6, v7
	v_add_u32_e32 v125, s14, v59
	ds_write_b32 v125, v6
	v_cvt_pk_bf16_f32 v8, v180, v181
	v_cvt_pk_bf16_f32 v9, v182, v183
	v_add_u32_e32 v10, s15, v76
	s_mov_b64 exec, s[48:49]
	ds_write_b64 v10, v[8:9]
	s_mov_b64 exec, -1
	s_waitcnt vmcnt(2)
	v_mul_f32_e32 v11, v117, v185
	v_mul_f32_e32 v15, v119, v187
	v_fmac_f32_e32 v11, v116, v184
	v_fmac_f32_e32 v15, v118, v186
	s_add_i32 s13, s2, 13
	s_and_b32 s13, s13, 15
	s_mul_i32 s14, s13, 0x104
	s_mul_i32 s15, s13, 0x110
	v_add_f32_e32 v11, v11, v15
	v_add_u32_e32 v16, s14, v59
	ds_write_b32 v16, v11
	v_cvt_pk_bf16_f32 v12, v184, v185
	v_cvt_pk_bf16_f32 v13, v186, v187
	v_add_u32_e32 v14, s15, v76
	s_mov_b64 exec, s[48:49]
	ds_write_b64 v14, v[12:13]
	s_mov_b64 exec, -1
	s_waitcnt vmcnt(1)
	v_mul_f32_e32 v6, v117, v189
	v_mul_f32_e32 v7, v119, v191
	v_fmac_f32_e32 v6, v116, v188
	v_fmac_f32_e32 v7, v118, v190
	s_add_i32 s13, s2, 14
	s_and_b32 s13, s13, 15
	s_mul_i32 s14, s13, 0x104
	s_mul_i32 s15, s13, 0x110
	v_add_f32_e32 v6, v6, v7
	v_add_u32_e32 v125, s14, v59
	ds_write_b32 v125, v6
	v_cvt_pk_bf16_f32 v8, v188, v189
	v_cvt_pk_bf16_f32 v9, v190, v191
	v_add_u32_e32 v10, s15, v76
	s_mov_b64 exec, s[48:49]
	ds_write_b64 v10, v[8:9]
	s_mov_b64 exec, -1
	s_waitcnt vmcnt(0)
	v_mul_f32_e32 v11, v117, v193
	v_mul_f32_e32 v15, v119, v195
	v_fmac_f32_e32 v11, v116, v192
	v_fmac_f32_e32 v15, v118, v194
	s_add_i32 s13, s2, 15
	s_and_b32 s13, s13, 15
	s_mul_i32 s14, s13, 0x104
	s_mul_i32 s15, s13, 0x110
	v_add_f32_e32 v11, v11, v15
	v_add_u32_e32 v16, s14, v59
	ds_write_b32 v16, v11
	v_cvt_pk_bf16_f32 v12, v192, v193
	v_cvt_pk_bf16_f32 v13, v194, v195
	v_add_u32_e32 v14, s15, v76
	s_mov_b64 exec, s[48:49]
	ds_write_b64 v14, v[12:13]
	s_mov_b64 exec, -1
	s_waitcnt lgkmcnt(0)
	ds_read2_b32 v[60:61], v77 offset0:0 offset1:1
	ds_read2_b32 v[62:63], v77 offset0:2 offset1:3
	ds_read2_b32 v[64:65], v77 offset0:4 offset1:5
	ds_read2_b32 v[66:67], v77 offset0:6 offset1:7
	ds_read2_b32 v[68:69], v77 offset0:8 offset1:9
	ds_read2_b32 v[70:71], v77 offset0:10 offset1:11
	ds_read2_b32 v[72:73], v77 offset0:12 offset1:13
	ds_read2_b32 v[74:75], v77 offset0:14 offset1:15
	s_waitcnt lgkmcnt(0)
	v_add_f32_e32 v78, 0, v60
	v_add_f32_e32 v78, v78, v61
	v_add_f32_e32 v78, v78, v62
	v_add_f32_e32 v78, v78, v63
	v_add_f32_e32 v78, v78, v64
	v_add_f32_e32 v78, v78, v65
	v_add_f32_e32 v78, v78, v66
	v_add_f32_e32 v78, v78, v67
	v_add_f32_e32 v78, v78, v68
	v_add_f32_e32 v78, v78, v69
	v_add_f32_e32 v78, v78, v70
	v_add_f32_e32 v78, v78, v71
	v_add_f32_e32 v78, v78, v72
	v_add_f32_e32 v78, v78, v73
	v_add_f32_e32 v78, v78, v74
	v_add_f32_e32 v78, v78, v75
	s_nop 1
	v_add_f32_dpp v78, v78, v78 quad_perm:[1,0,3,2] row_mask:0xf bank_mask:0xf bound_ctrl:1
	s_nop 1
	v_add_f32_dpp v78, v78, v78 quad_perm:[2,3,0,1] row_mask:0xf bank_mask:0xf bound_ctrl:1
	v_lshlrev_b32_e32 v79, 4, v1
	ds_bpermute_b32 v78, v79, v78
	s_waitcnt lgkmcnt(0)
	s_barrier
	global_load_dwordx4 v[2:5], v123, s[34:35] nt
	global_load_dwordx4 v[6:9], v123, s[34:35] offset:1024 nt
	global_load_dwordx4 v[10:13], v123, s[34:35] offset:2048 nt
	global_load_dwordx4 v[14:17], v123, s[34:35] offset:3072 nt
	ds_read_b128 v[28:31], v53
	ds_read_b128 v[60:63], v56
	ds_read_b128 v[32:35], v53 offset:64
	ds_read_b128 v[64:67], v56 offset:64
	ds_read_b128 v[36:39], v53 offset:128
	ds_read_b128 v[68:71], v56 offset:128
	ds_read_b128 v[40:43], v53 offset:192
	ds_read_b128 v[72:75], v56 offset:192
	s_waitcnt lgkmcnt(6)
	v_mfma_f32_16x16x32_bf16 v[18:21], v[28:31], v[60:63], 0
	s_waitcnt lgkmcnt(4)
	v_mfma_f32_16x16x32_bf16 v[18:21], v[32:35], v[64:67], v[18:21]
	s_waitcnt lgkmcnt(2)
	v_mfma_f32_16x16x32_bf16 v[18:21], v[36:39], v[68:71], v[18:21]
	s_waitcnt lgkmcnt(0)
	v_mfma_f32_16x16x32_bf16 v[18:21], v[40:43], v[72:75], v[18:21]
	s_nop 7
	v_mul_f32_e32 v18, s44, v18
	v_mul_f32_e32 v19, s44, v19
	v_mul_f32_e32 v20, s44, v20
	v_mul_f32_e32 v21, s44, v21
	v_cvt_pk_bf16_f32 v18, v18, v18
	v_cvt_pk_bf16_f32 v19, v19, v19
	v_cvt_pk_bf16_f32 v20, v20, v20
	v_cvt_pk_bf16_f32 v21, v21, v21
	ds_write_b16 v55, v18
	ds_write_b16 v55, v19 offset:272
	ds_write_b16 v55, v20 offset:544
	ds_write_b16 v55, v21 offset:816
	s_waitcnt lgkmcnt(0)
	s_barrier
	ds_read_b128 v[28:31], v54
	ds_read_b128 v[60:63], v57
	ds_read_b128 v[32:35], v54 offset:64
	ds_read_b128 v[64:67], v57 offset:64
	ds_read_b128 v[36:39], v54 offset:128
	ds_read_b128 v[68:71], v57 offset:128
	ds_read_b128 v[40:43], v54 offset:192
	ds_read_b128 v[72:75], v57 offset:192
	s_waitcnt lgkmcnt(6)
	v_mfma_f32_16x16x32_bf16 v[18:21], v[28:31], v[60:63], 0
	s_waitcnt lgkmcnt(4)
	v_mfma_f32_16x16x32_bf16 v[18:21], v[32:35], v[64:67], v[18:21]
	s_waitcnt lgkmcnt(2)
	v_mfma_f32_16x16x32_bf16 v[18:21], v[36:39], v[68:71], v[18:21]
	s_waitcnt lgkmcnt(0)
	v_mfma_f32_16x16x32_bf16 v[18:21], v[40:43], v[72:75], v[18:21]
	s_nop 2
	v_mov_b32_e32 v28, v78
	s_load_dwordx2 s[4:5], s[0:1], 0x70
	v_lshl_or_b32 v30, v24, 2, s3
	v_ashrrev_i32_e32 v31, 31, v30
	v_mov_b32_e32 v107, 0
	s_waitcnt lgkmcnt(0)
	v_add_f32_e32 v34, v130, v28
	v_add_f32_e32 v35, v34, v18
	v_add_f32_e32 v28, v35, v35
	v_mul_f32_e32 v28, 0x3fb8aa3b, v28
	v_exp_f32_e32 v32, v28
	v_lshlrev_b64 v[28:29], 9, v[30:31]
	s_mov_b32 s8, 0x19200
	v_add3_u32 v37, v27, v25, s8
	v_add_f32_e32 v31, 1.0, v32
	v_rcp_f32_e32 v31, v31
	v_lshl_add_u64 v[32:33], s[4:5], 0, v[106:107]
	v_lshl_add_u64 v[28:29], v[32:33], 0, v[28:29]
	global_store_dword v[28:29], v35, off sc1
	v_fma_f32 v35, v31, -2.0, 1.0
	v_fma_f32 v28, -v35, v35, 1.0
	v_mul_f32_e32 v28, v129, v28
	v_add_f32_e32 v31, v34, v19
	v_cvt_pk_bf16_f32 v29, v28, s0
	v_mul_f32_e64 v27, v35, -v28
	v_add_f32_e32 v28, v31, v31
	v_mul_f32_e32 v28, 0x3fb8aa3b, v28
	v_exp_f32_e32 v38, v28
	v_cvt_pk_bf16_f32 v27, v27, s0
	ds_write_b16 v37, v27 offset:4352
	v_or_b32_e32 v28, 1, v30
	v_add_f32_e32 v27, 1.0, v38
	v_rcp_f32_e32 v27, v27
	ds_write_b16 v37, v29
	v_ashrrev_i32_e32 v29, 31, v28
	v_lshlrev_b64 v[28:29], 9, v[28:29]
	v_lshl_add_u64 v[28:29], v[32:33], 0, v[28:29]
	v_fma_f32 v27, v27, -2.0, 1.0
	global_store_dword v[28:29], v31, off sc1
	v_fma_f32 v28, -v27, v27, 1.0
	v_mul_f32_e32 v28, v129, v28
	v_cvt_pk_bf16_f32 v29, v28, s0
	v_add_f32_e32 v31, v34, v20
	ds_write_b16 v37, v29 offset:272
	v_add_f32_e32 v29, v31, v31
	v_mul_f32_e32 v29, 0x3fb8aa3b, v29
	v_exp_f32_e32 v38, v29
	v_mul_f32_e64 v28, v27, -v28
	v_cvt_pk_bf16_f32 v28, v28, s0
	ds_write_b16 v37, v28 offset:4624
	v_add_f32_e32 v38, 1.0, v38
	v_or_b32_e32 v28, 2, v30
	v_rcp_f32_e32 v38, v38
	v_ashrrev_i32_e32 v29, 31, v28
	v_lshlrev_b64 v[28:29], 9, v[28:29]
	v_lshl_add_u64 v[28:29], v[32:33], 0, v[28:29]
	global_store_dword v[28:29], v31, off sc1
	v_fma_f32 v28, v38, -2.0, 1.0
	v_fma_f32 v29, -v28, v28, 1.0
	v_mul_f32_e32 v29, v129, v29
	v_cvt_pk_bf16_f32 v31, v29, s0
	v_add_f32_e32 v34, v34, v21
	ds_write_b16 v37, v31 offset:544
	v_add_f32_e32 v31, v34, v34
	v_mul_f32_e32 v31, 0x3fb8aa3b, v31
	v_exp_f32_e32 v38, v31
	v_mul_f32_e64 v29, v28, -v29
	v_cvt_pk_bf16_f32 v29, v29, s0
	ds_write_b16 v37, v29 offset:4896
	v_add_f32_e32 v29, 1.0, v38
	v_rcp_f32_e32 v29, v29
	v_or_b32_e32 v30, 3, v30
	v_ashrrev_i32_e32 v31, 31, v30
	v_lshlrev_b64 v[30:31], 9, v[30:31]
	v_lshl_add_u64 v[30:31], v[32:33], 0, v[30:31]
	v_fma_f32 v29, v29, -2.0, 1.0
	global_store_dword v[30:31], v34, off sc1
	v_fma_f32 v30, -v29, v29, 1.0
	v_mul_f32_e32 v30, v129, v30
	v_cvt_pk_bf16_f32 v31, v30, s0
	v_mul_f32_e64 v30, v29, -v30
	v_cvt_pk_bf16_f32 v30, v30, s0
	ds_write_b16 v37, v30 offset:5168
	v_mov_b32_e32 v30, 0x1d800
	v_mul_f32_e32 v36, v129, v35
	v_lshl_or_b32 v32, v128, 6, v30
	v_mov_b32_e32 v30, v107
	ds_write_b16 v37, v31 offset:816
	v_mov_b32_e32 v31, 0
	v_mov_b32_dpp v30, v36 quad_perm:[1,0,3,2] row_mask:0xf bank_mask:0xf
	v_fmac_f32_e32 v30, v129, v35
	v_cmp_eq_u32_e32 vcc, 0, v1
	v_add_u32_e32 v26, v32, v26
	v_add_f32_dpp v30, v30, v30 quad_perm:[2,3,0,1] row_mask:0xf bank_mask:0xf bound_ctrl:1
	s_nop 1
	v_add_f32_dpp v30, v30, v30 row_half_mirror row_mask:0xf bank_mask:0xf bound_ctrl:1
	s_nop 1
	v_mov_b32_dpp v31, v30 row_mirror row_mask:0xf bank_mask:0xf
	s_and_saveexec_b64 s[4:5], vcc
	v_add_f32_e32 v30, v30, v31
	ds_write_b32 v26, v30
	s_or_b64 exec, exec, s[4:5]
	v_mul_f32_e32 v30, v129, v27
	v_mov_b32_e32 v31, 0
	s_nop 1
	v_mov_b32_dpp v31, v30 quad_perm:[1,0,3,2] row_mask:0xf bank_mask:0xf
	v_fmac_f32_e32 v31, v129, v27
	s_nop 1
	v_add_f32_dpp v27, v31, v31 quad_perm:[2,3,0,1] row_mask:0xf bank_mask:0xf bound_ctrl:1
	s_nop 1
	v_add_f32_dpp v27, v27, v27 row_half_mirror row_mask:0xf bank_mask:0xf bound_ctrl:1
	s_nop 1
	v_mov_b32_dpp v107, v27 row_mirror row_mask:0xf bank_mask:0xf
	s_and_saveexec_b64 s[4:5], vcc
	v_add_f32_e32 v27, v27, v107
	ds_write_b32 v26, v27 offset:4
	s_or_b64 exec, exec, s[4:5]
	v_mul_f32_e32 v30, v129, v28
	v_mov_b32_e32 v31, 0
	v_mov_b32_e32 v27, 0
	s_nop 0
	v_mov_b32_dpp v31, v30 quad_perm:[1,0,3,2] row_mask:0xf bank_mask:0xf
	v_fmac_f32_e32 v31, v129, v28
	v_mov_b32_e32 v30, 0
	s_nop 0
	v_add_f32_dpp v28, v31, v31 quad_perm:[2,3,0,1] row_mask:0xf bank_mask:0xf bound_ctrl:1
	s_nop 1
	v_add_f32_dpp v28, v28, v28 row_half_mirror row_mask:0xf bank_mask:0xf bound_ctrl:1
	s_nop 1
	v_mov_b32_dpp v30, v28 row_mirror row_mask:0xf bank_mask:0xf
	s_and_saveexec_b64 s[4:5], vcc
	v_add_f32_e32 v28, v28, v30
	ds_write_b32 v26, v28 offset:8
	s_or_b64 exec, exec, s[4:5]
	v_mul_f32_e32 v28, v129, v29
	v_mov_b32_e32 v30, 0
	s_nop 1
	v_mov_b32_dpp v30, v28 quad_perm:[1,0,3,2] row_mask:0xf bank_mask:0xf
	v_fmac_f32_e32 v30, v129, v29
	s_nop 1
	v_add_f32_dpp v28, v30, v30 quad_perm:[2,3,0,1] row_mask:0xf bank_mask:0xf bound_ctrl:1
	s_nop 1
	v_add_f32_dpp v28, v28, v28 row_half_mirror row_mask:0xf bank_mask:0xf bound_ctrl:1
	s_nop 1
	v_mov_b32_dpp v27, v28 row_mirror row_mask:0xf bank_mask:0xf
	s_and_saveexec_b64 s[4:5], vcc
	v_add_f32_e32 v27, v28, v27
	ds_write_b32 v26, v27 offset:12
	s_or_b64 exec, exec, s[4:5]
	s_mov_b64 s[4:5], 0
	s_branch .LBB0_28
.Lp_q:
	v_lshrrev_b32_e32 v122, 5, v0
	v_lshlrev_b32_e32 v122, 10, v122
	v_and_b32_e32 v125, 31, v0
	v_lshl_add_u32 v122, v125, 4, v122
	s_and_b32 s13, s2, 7
	s_lshl_b32 s14, s13, 14
	v_add_u32_e32 v125, s14, v122
	global_load_dwordx4 v[132:135], v125, s[28:29]
	s_add_i32 s13, s2, 1
	s_and_b32 s13, s13, 7
	s_lshl_b32 s14, s13, 14
	v_add_u32_e32 v125, s14, v122
	global_load_dwordx4 v[136:139], v125, s[28:29]
	s_add_i32 s13, s2, 2
	s_and_b32 s13, s13, 7
	s_lshl_b32 s14, s13, 14
	v_add_u32_e32 v125, s14, v122
	global_load_dwordx4 v[140:143], v125, s[28:29]
	s_add_i32 s13, s2, 3
	s_and_b32 s13, s13, 7
	s_lshl_b32 s14, s13, 14
	v_add_u32_e32 v125, s14, v122
	global_load_dwordx4 v[144:147], v125, s[28:29]
	s_add_i32 s13, s2, 4
	s_and_b32 s13, s13, 7
	s_lshl_b32 s14, s13, 14
	v_add_u32_e32 v125, s14, v122
	global_load_dwordx4 v[148:151], v125, s[28:29]
	s_add_i32 s13, s2, 5
	s_and_b32 s13, s13, 7
	s_lshl_b32 s14, s13, 14
	v_add_u32_e32 v125, s14, v122
	global_load_dwordx4 v[152:155], v125, s[28:29]
	s_add_i32 s13, s2, 6
	s_and_b32 s13, s13, 7
	s_lshl_b32 s14, s13, 14
	v_add_u32_e32 v125, s14, v122
	global_load_dwordx4 v[156:159], v125, s[28:29]
	s_add_i32 s13, s2, 7
	s_and_b32 s13, s13, 7
	s_lshl_b32 s14, s13, 14
	v_add_u32_e32 v125, s14, v122
	global_load_dwordx4 v[160:163], v125, s[28:29]
	s_waitcnt vmcnt(18)
	v_cvt_pk_bf16_f32 v12, v2, v3
	v_cvt_pk_bf16_f32 v13, v4, v5
	ds_write_b64 v124, v[12:13]
	s_waitcnt vmcnt(17)
	v_cvt_pk_bf16_f32 v6, v80, v81
	v_cvt_pk_bf16_f32 v7, v82, v83
	s_and_b32 s13, s2, 7
	s_mul_i32 s14, s13, 0x1100
	v_add_u32_e32 v125, s14, v58
	ds_write_b64 v125, v[6:7]
	s_waitcnt vmcnt(16)
	v_cvt_pk_bf16_f32 v8, v84, v85
	v_cvt_pk_bf16_f32 v9, v86, v87
	s_add_i32 s13, s2, 1
	s_and_b32 s13, s13, 7
	s_mul_i32 s14, s13, 0x1100
	v_add_u32_e32 v10, s14, v58
	ds_write_b64 v10, v[8:9]
	s_waitcnt vmcnt(15)
	v_cvt_pk_bf16_f32 v6, v88, v89
	v_cvt_pk_bf16_f32 v7, v90, v91
	s_add_i32 s13, s2, 2
	s_and_b32 s13, s13, 7
	s_mul_i32 s14, s13, 0x1100
	v_add_u32_e32 v125, s14, v58
	ds_write_b64 v125, v[6:7]
	s_waitcnt vmcnt(14)
	v_cvt_pk_bf16_f32 v8, v92, v93
	v_cvt_pk_bf16_f32 v9, v94, v95
	s_add_i32 s13, s2, 3
	s_and_b32 s13, s13, 7
	s_mul_i32 s14, s13, 0x1100
	v_add_u32_e32 v10, s14, v58
	ds_write_b64 v10, v[8:9]
	s_waitcnt vmcnt(13)
	v_cvt_pk_bf16_f32 v6, v96, v97
	v_cvt_pk_bf16_f32 v7, v98, v99
	s_add_i32 s13, s2, 4
	s_and_b32 s13, s13, 7
	s_mul_i32 s14, s13, 0x1100
	v_add_u32_e32 v125, s14, v58
	ds_write_b64 v125, v[6:7]
	s_waitcnt vmcnt(12)
	v_cvt_pk_bf16_f32 v8, v100, v101
	v_cvt_pk_bf16_f32 v9, v102, v103
	s_add_i32 s13, s2, 5
	s_and_b32 s13, s13, 7
	s_mul_i32 s14, s13, 0x1100
	v_add_u32_e32 v10, s14, v58
	ds_write_b64 v10, v[8:9]
	s_waitcnt vmcnt(11)
	v_cvt_pk_bf16_f32 v6, v108, v109
	v_cvt_pk_bf16_f32 v7, v110, v111
	s_add_i32 s13, s2, 6
	s_and_b32 s13, s13, 7
	s_mul_i32 s14, s13, 0x1100
	v_add_u32_e32 v125, s14, v58
	ds_write_b64 v125, v[6:7]
	s_waitcnt vmcnt(10)
	v_cvt_pk_bf16_f32 v8, v112, v113
	v_cvt_pk_bf16_f32 v9, v114, v115
	s_add_i32 s13, s2, 7
	s_and_b32 s13, s13, 7
	s_mul_i32 s14, s13, 0x1100
	v_add_u32_e32 v10, s14, v58
	ds_write_b64 v10, v[8:9]
	s_waitcnt vmcnt(7)
	v_cvt_pk_bf16_f32 v6, v132, v133
	v_cvt_pk_bf16_f32 v7, v134, v135
	s_and_b32 s13, s2, 7
	s_mul_i32 s14, s13, 0x1100
	s_add_i32 s14, s14, 34816
	v_add_u32_e32 v125, s14, v58
	ds_write_b64 v125, v[6:7]
	s_waitcnt vmcnt(6)
	v_cvt_pk_bf16_f32 v8, v136, v137
	v_cvt_pk_bf16_f32 v9, v138, v139
	s_add_i32 s13, s2, 1
	s_and_b32 s13, s13, 7
	s_mul_i32 s14, s13, 0x1100
	s_add_i32 s14, s14, 34816
	v_add_u32_e32 v10, s14, v58
	ds_write_b64 v10, v[8:9]
	s_waitcnt vmcnt(5)
	v_cvt_pk_bf16_f32 v6, v140, v141
	v_cvt_pk_bf16_f32 v7, v142, v143
	s_add_i32 s13, s2, 2
	s_and_b32 s13, s13, 7
	s_mul_i32 s14, s13, 0x1100
	s_add_i32 s14, s14, 34816
	v_add_u32_e32 v125, s14, v58
	ds_write_b64 v125, v[6:7]
	s_waitcnt vmcnt(4)
	v_cvt_pk_bf16_f32 v8, v144, v145
	v_cvt_pk_bf16_f32 v9, v146, v147
	s_add_i32 s13, s2, 3
	s_and_b32 s13, s13, 7
	s_mul_i32 s14, s13, 0x1100
	s_add_i32 s14, s14, 34816
	v_add_u32_e32 v10, s14, v58
	ds_write_b64 v10, v[8:9]
	s_waitcnt vmcnt(3)
	v_cvt_pk_bf16_f32 v6, v148, v149
	v_cvt_pk_bf16_f32 v7, v150, v151
	s_add_i32 s13, s2, 4
	s_and_b32 s13, s13, 7
	s_mul_i32 s14, s13, 0x1100
	s_add_i32 s14, s14, 34816
	v_add_u32_e32 v125, s14, v58
	ds_write_b64 v125, v[6:7]
	s_waitcnt vmcnt(2)
	v_cvt_pk_bf16_f32 v8, v152, v153
	v_cvt_pk_bf16_f32 v9, v154, v155
	s_add_i32 s13, s2, 5
	s_and_b32 s13, s13, 7
	s_mul_i32 s14, s13, 0x1100
	s_add_i32 s14, s14, 34816
	v_add_u32_e32 v10, s14, v58
	ds_write_b64 v10, v[8:9]
	s_waitcnt vmcnt(1)
	v_cvt_pk_bf16_f32 v6, v156, v157
	v_cvt_pk_bf16_f32 v7, v158, v159
	s_add_i32 s13, s2, 6
	s_and_b32 s13, s13, 7
	s_mul_i32 s14, s13, 0x1100
	s_add_i32 s14, s14, 34816
	v_add_u32_e32 v125, s14, v58
	ds_write_b64 v125, v[6:7]
	s_waitcnt vmcnt(0)
	v_cvt_pk_bf16_f32 v8, v160, v161
	v_cvt_pk_bf16_f32 v9, v162, v163
	s_add_i32 s13, s2, 7
	s_and_b32 s13, s13, 7
	s_mul_i32 s14, s13, 0x1100
	s_add_i32 s14, s14, 34816
	v_add_u32_e32 v10, s14, v58
	ds_write_b64 v10, v[8:9]
	s_waitcnt lgkmcnt(0)
	s_barrier
	global_load_dwordx4 v[2:5], v123, s[34:35] nt
	global_load_dwordx4 v[6:9], v123, s[34:35] offset:1024 nt
	global_load_dwordx4 v[10:13], v123, s[34:35] offset:2048 nt
	global_load_dwordx4 v[14:17], v123, s[34:35] offset:3072 nt
	ds_read_b128 v[28:31], v53
	ds_read_b128 v[60:63], v56
	ds_read_b128 v[32:35], v53 offset:64
	ds_read_b128 v[64:67], v56 offset:64
	ds_read_b128 v[36:39], v53 offset:128
	ds_read_b128 v[68:71], v56 offset:128
	ds_read_b128 v[40:43], v53 offset:192
	ds_read_b128 v[72:75], v56 offset:192
	s_waitcnt lgkmcnt(6)
	v_mfma_f32_16x16x32_bf16 v[18:21], v[28:31], v[60:63], 0
	s_waitcnt lgkmcnt(4)
	v_mfma_f32_16x16x32_bf16 v[18:21], v[32:35], v[64:67], v[18:21]
	s_waitcnt lgkmcnt(2)
	v_mfma_f32_16x16x32_bf16 v[18:21], v[36:39], v[68:71], v[18:21]
	s_waitcnt lgkmcnt(0)
	v_mfma_f32_16x16x32_bf16 v[18:21], v[40:43], v[72:75], v[18:21]
	s_nop 7
	v_mul_f32_e32 v18, s44, v18
	v_mul_f32_e32 v19, s44, v19
	v_mul_f32_e32 v20, s44, v20
	v_mul_f32_e32 v21, s44, v21
	v_cvt_pk_bf16_f32 v18, v18, v18
	v_cvt_pk_bf16_f32 v19, v19, v19
	v_cvt_pk_bf16_f32 v20, v20, v20
	v_cvt_pk_bf16_f32 v21, v21, v21
	ds_write_b16 v55, v18
	ds_write_b16 v55, v19 offset:272
	ds_write_b16 v55, v20 offset:544
	ds_write_b16 v55, v21 offset:816
	s_waitcnt lgkmcnt(0)
	s_barrier
	ds_read_b128 v[28:31], v54
	ds_read_b128 v[60:63], v57
	ds_read_b128 v[32:35], v54 offset:64
	ds_read_b128 v[64:67], v57 offset:64
	ds_read_b128 v[36:39], v54 offset:128
	ds_read_b128 v[68:71], v57 offset:128
	ds_read_b128 v[40:43], v54 offset:192
	ds_read_b128 v[72:75], v57 offset:192
	s_waitcnt lgkmcnt(6)
	v_mfma_f32_16x16x32_bf16 v[18:21], v[28:31], v[60:63], 0
	s_waitcnt lgkmcnt(4)
	v_mfma_f32_16x16x32_bf16 v[18:21], v[32:35], v[64:67], v[18:21]
	s_waitcnt lgkmcnt(2)
	v_mfma_f32_16x16x32_bf16 v[18:21], v[36:39], v[68:71], v[18:21]
	s_waitcnt lgkmcnt(0)
	v_mfma_f32_16x16x32_bf16 v[18:21], v[40:43], v[72:75], v[18:21]
	s_load_dwordx2 s[4:5], s[0:1], 0x68
	v_lshl_or_b32 v26, v24, 2, s12
	v_mov_b32_e32 v107, 0
	v_ashrrev_i32_e32 v27, 31, v26
	v_lshlrev_b64 v[28:29], 9, v[26:27]
	s_waitcnt lgkmcnt(0)
	v_lshl_add_u64 v[30:31], s[4:5], 0, v[106:107]
	v_lshl_add_u64 v[28:29], v[30:31], 0, v[28:29]
	v_mul_u32_u24_e32 v24, 0x440, v24
	s_mov_b32 s4, 0x19200
	global_store_dword v[28:29], v18, off sc1
	v_add3_u32 v28, v24, v25, s4
	v_mul_f32_e32 v24, v18, v18
	v_cvt_pk_bf16_f32 v27, v18, s0
	v_cvt_pk_bf16_f32 v24, v24, s0
	ds_write_b16 v28, v27
	ds_write_b16 v28, v24 offset:4352
	v_max3_f32 v27, |v18|, 0, |v19|
	v_or_b32_e32 v24, 1, v26
	v_cvt_pk_bf16_f32 v18, v19, s0
	v_ashrrev_i32_e32 v25, 31, v24
	ds_write_b16 v28, v18 offset:272
	v_mul_f32_e32 v18, v19, v19
	v_lshlrev_b64 v[24:25], 9, v[24:25]
	v_cvt_pk_bf16_f32 v18, v18, s0
	v_lshl_add_u64 v[24:25], v[30:31], 0, v[24:25]
	ds_write_b16 v28, v18 offset:4624
	v_or_b32_e32 v18, 2, v26
	global_store_dword v[24:25], v19, off sc1
	v_ashrrev_i32_e32 v19, 31, v18
	v_lshlrev_b64 v[18:19], 9, v[18:19]
	v_lshl_add_u64 v[18:19], v[30:31], 0, v[18:19]
	global_store_dword v[18:19], v20, off sc1
	v_cvt_pk_bf16_f32 v18, v20, s0
	ds_write_b16 v28, v18 offset:544
	v_mul_f32_e32 v18, v20, v20
	v_cvt_pk_bf16_f32 v18, v18, s0
	ds_write_b16 v28, v18 offset:4896
	v_or_b32_e32 v18, 3, v26
	v_ashrrev_i32_e32 v19, 31, v18
	v_lshlrev_b64 v[18:19], 9, v[18:19]
	v_lshl_add_u64 v[18:19], v[30:31], 0, v[18:19]
	global_store_dword v[18:19], v21, off sc1
	v_cvt_pk_bf16_f32 v18, v21, s0
	ds_write_b16 v28, v18 offset:816
	v_mul_f32_e32 v18, v21, v21
	v_cvt_pk_bf16_f32 v18, v18, s0
	v_max3_f32 v20, v27, |v20|, |v21|
	ds_write_b16 v28, v18 offset:5168
	v_mov_b32_e32 v18, v107
	v_mov_b32_e32 v19, v107
	v_cmp_eq_u32_e32 vcc, 0, v126
	v_mov_b32_dpp v18, v20 quad_perm:[1,0,3,2] row_mask:0xf bank_mask:0xf
	v_max_f32_e32 v18, v18, v18
	v_max_f32_e32 v18, v20, v18
	s_nop 1
	v_mov_b32_dpp v19, v18 quad_perm:[2,3,0,1] row_mask:0xf bank_mask:0xf
	v_max_f32_e32 v19, v19, v19
	v_max_f32_e32 v18, v18, v19
	v_mov_b32_e32 v19, v107
	s_nop 1
	v_mov_b32_dpp v19, v18 row_half_mirror row_mask:0xf bank_mask:0xf
	v_max_f32_e32 v19, v19, v19
	v_max_f32_e32 v18, v18, v19
	v_mov_b32_e32 v19, v107
	s_nop 1
	v_mov_b32_dpp v19, v18 row_mirror row_mask:0xf bank_mask:0xf
	v_max_f32_e32 v19, v19, v19
	v_max_f32_e32 v18, v18, v19
	s_nop 0
	v_readlane_b32 s8, v18, 0
	v_readlane_b32 s9, v18, 16
	v_readlane_b32 s10, v18, 32
	v_readlane_b32 s11, v18, 48
	v_and_b32_e32 v18, 0x7fffffff, v129
	s_nop 1
	v_add_f32_dpp v18, v18, |v129| quad_perm:[1,0,3,2] row_mask:0xf bank_mask:0xf bound_ctrl:1
	s_nop 1
	v_add_f32_dpp v18, v18, v18 quad_perm:[2,3,0,1] row_mask:0xf bank_mask:0xf bound_ctrl:1
	s_nop 1
	v_add_f32_dpp v18, v18, v18 row_half_mirror row_mask:0xf bank_mask:0xf bound_ctrl:1
	s_nop 1
	v_mov_b32_dpp v107, v18 row_mirror row_mask:0xf bank_mask:0xf
	s_and_saveexec_b64 s[4:5], vcc
	s_cbranch_execz .LBB0_27
	v_mov_b32_e32 v19, 0x1d800
	v_lshl_or_b32 v20, v128, 6, v19
	v_add_f32_e32 v19, v18, v107
	v_max_f32_e64 v18, s11, s11
	v_max_f32_e64 v21, s10, s10
	v_max_f32_e32 v18, v21, v18
	v_mov_b32_e32 v21, s9
	v_max3_f32 v18, s8, v21, v18
	ds_write_b64 v20, v[18:19]

	.amdhsa_kernel _Z11prep_kernelPKfS0_S0_S0_S0_S0_S0_S0_S0_PKiPDv8_DF16bS4_PfS5_S5_PiPt
		.amdhsa_group_segment_fixed_size 121344
		.amdhsa_private_segment_fixed_size 0
		.amdhsa_kernarg_size 136
		.amdhsa_user_sgpr_count 2
		.amdhsa_user_sgpr_dispatch_ptr 0
		.amdhsa_user_sgpr_queue_ptr 0
		.amdhsa_user_sgpr_kernarg_segment_ptr 1
		.amdhsa_user_sgpr_dispatch_id 0
		.amdhsa_user_sgpr_kernarg_preload_length 0
		.amdhsa_user_sgpr_kernarg_preload_offset 0
		.amdhsa_user_sgpr_private_segment_size 0
		.amdhsa_uses_dynamic_stack 0
		.amdhsa_enable_private_segment 0
		.amdhsa_system_sgpr_workgroup_id_x 1
		.amdhsa_system_sgpr_workgroup_id_y 0
		.amdhsa_system_sgpr_workgroup_id_z 0
		.amdhsa_system_sgpr_workgroup_info 0
		.amdhsa_system_vgpr_workitem_id 0
		.amdhsa_next_free_vgpr 200
		.amdhsa_next_free_sgpr 96
		.amdhsa_accum_offset 200
		.amdhsa_reserve_vcc 1
		.amdhsa_float_round_mode_32 0
		.amdhsa_float_round_mode_16_64 0
		.amdhsa_float_denorm_mode_32 3
		.amdhsa_float_denorm_mode_16_64 3
		.amdhsa_dx10_clamp 1
		.amdhsa_ieee_mode 1
		.amdhsa_fp16_overflow 0
		.amdhsa_tg_split 0
		.amdhsa_exception_fp_ieee_invalid_op 0
		.amdhsa_exception_fp_denorm_src 0
		.amdhsa_exception_fp_ieee_div_zero 0
		.amdhsa_exception_fp_ieee_overflow 0
		.amdhsa_exception_fp_ieee_underflow 0
		.amdhsa_exception_fp_ieee_inexact 0
		.amdhsa_exception_int_div_zero 0
	.end_amdhsa_kernel

amdhsa.kernels:
  - .agpr_count:     0
    .args:
      - .actual_access:  read_only
        .address_space:  global
        .offset:         0
        .size:           8
        .value_kind:     global_buffer
      - .actual_access:  read_only
        .address_space:  global
        .offset:         8
        .size:           8
        .value_kind:     global_buffer
      - .actual_access:  read_only
        .address_space:  global
        .offset:         16
        .size:           8
        .value_kind:     global_buffer
      - .actual_access:  read_only
        .address_space:  global
        .offset:         24
        .size:           8
        .value_kind:     global_buffer
      - .actual_access:  read_only
        .address_space:  global
        .offset:         32
        .size:           8
        .value_kind:     global_buffer
      - .actual_access:  read_only
        .address_space:  global
        .offset:         40
        .size:           8
        .value_kind:     global_buffer
      - .actual_access:  read_only
        .address_space:  global
        .offset:         48
        .size:           8
        .value_kind:     global_buffer
      - .actual_access:  read_only
        .address_space:  global
        .offset:         56
        .size:           8
        .value_kind:     global_buffer
      - .actual_access:  read_only
        .address_space:  global
        .offset:         64
        .size:           8
        .value_kind:     global_buffer
      - .actual_access:  read_only
        .address_space:  global
        .offset:         72
        .size:           8
        .value_kind:     global_buffer
      - .actual_access:  write_only
        .address_space:  global
        .offset:         80
        .size:           8
        .value_kind:     global_buffer
      - .actual_access:  write_only
        .address_space:  global
        .offset:         88
        .size:           8
        .value_kind:     global_buffer
      - .actual_access:  write_only
        .address_space:  global
        .offset:         96
        .size:           8
        .value_kind:     global_buffer
      - .actual_access:  write_only
        .address_space:  global
        .offset:         104
        .size:           8
        .value_kind:     global_buffer
      - .actual_access:  write_only
        .address_space:  global
        .offset:         112
        .size:           8
        .value_kind:     global_buffer
      - .actual_access:  write_only
        .address_space:  global
        .offset:         120
        .size:           8
        .value_kind:     global_buffer
      - .actual_access:  write_only
        .address_space:  global
        .offset:         128
        .size:           8
        .value_kind:     global_buffer
    .group_segment_fixed_size: 121344
    .kernarg_segment_align: 8
    .kernarg_segment_size: 136
    .language:       OpenCL C
    .language_version:
      - 2
      - 0
    .max_flat_workgroup_size: 512
    .name:           _Z11prep_kernelPKfS0_S0_S0_S0_S0_S0_S0_S0_PKiPDv8_DF16bS4_PfS5_S5_PiPt
    .private_segment_fixed_size: 0
    .sgpr_count:     31
    .sgpr_spill_count: 0
    .symbol:         _Z11prep_kernelPKfS0_S0_S0_S0_S0_S0_S0_S0_PKiPDv8_DF16bS4_PfS5_S5_PiPt.kd
    .uniform_work_group_size: 1
    .uses_dynamic_stack: false
    .vgpr_count:     200
    .vgpr_spill_count: 0
    .wavefront_size: 64
  - .agpr_count:     0
    .args:
      - .actual_access:  read_only
        .address_space:  global
        .offset:         0
        .size:           8
        .value_kind:     global_buffer
      - .actual_access:  read_only
        .address_space:  global
        .offset:         8
        .size:           8
        .value_kind:     global_buffer
      - .actual_access:  read_only
        .address_space:  global
        .offset:         16
        .size:           8
        .value_kind:     global_buffer
      - .actual_access:  read_only
        .address_space:  global
        .offset:         24
        .size:           8
        .value_kind:     global_buffer
      - .actual_access:  read_only
        .address_space:  global
        .offset:         32
        .size:           8
        .value_kind:     global_buffer
      - .actual_access:  read_only
        .address_space:  global
        .offset:         40
        .size:           8
        .value_kind:     global_buffer
      - .actual_access:  read_only
        .address_space:  global
        .offset:         48
        .size:           8
        .value_kind:     global_buffer
      - .actual_access:  read_only
        .address_space:  global
        .offset:         56
        .size:           8
        .value_kind:     global_buffer
      - .actual_access:  read_only
        .address_space:  global
        .offset:         64
        .size:           8
        .value_kind:     global_buffer
      - .actual_access:  write_only
        .address_space:  global
        .offset:         72
        .size:           8
        .value_kind:     global_buffer
    .group_segment_fixed_size: 70400
    .kernarg_segment_align: 8
    .kernarg_segment_size: 80
    .language:       OpenCL C
    .language_version:
      - 2
      - 0
    .max_flat_workgroup_size: 512
    .name:           _Z11main_kernelPKDv8_DF16bS1_PKfS3_S3_PKiPKtS3_S3_Pf
    .private_segment_fixed_size: 0
    .sgpr_count:     54
    .sgpr_spill_count: 0
    .symbol:         _Z11main_kernelPKDv8_DF16bS1_PKfS3_S3_PKiPKtS3_S3_Pf.kd
    .uniform_work_group_size: 1
    .uses_dynamic_stack: false
    .vgpr_count:     204
    .vgpr_spill_count: 0
    .wavefront_size: 64
